# baseline (speedup 1.0000x reference)
_Z6k_gemmPKfS0_PK15HIP_vector_typeIjLj4EEPDF16_PKh:
	s_load_dwordx4 s[20:23], s[0:1], 0x0
	s_load_dwordx4 s[4:7], s[0:1], 0x10
	s_load_dwordx2 s[38:39], s[0:1], 0x20
	v_readfirstlane_b32 s8, v0
	v_and_b32_e32 v1, 63, v0
	s_nop 3
	s_lshr_b32 s8, s8, 6
	s_and_b32 s40, s2, 7
	s_lshr_b32 s41, s2, 3
	s_mul_i32 s18, s40, 0x187
	s_add_u32 s19, s18, 0x187
	s_min_u32 s19, s19, 0xc35
	s_sub_u32 s33, s19, s18
	s_sub_u32 s33, s33, 0x180
	s_lshl_b32 s33, s33, 2
	s_cmp_lt_u32 s41, s33
	s_cselect_b32 s44, 7, 6
	s_lshr_b32 s45, s41, 2
	s_add_u32 s45, s45, s18
	s_add_u32 s45, s45, 0x180
	s_lshl_b32 s45, s45, 4
	s_and_b32 s46, s41, 3
	s_lshl_b32 s46, s46, 2
	s_add_u32 s47, s45, s46
	s_mul_i32 s45, s47, 0x4b0
	s_lshl_b32 s46, s47, 8
	s_add_i32 s18, s18, s41
	s_cmp_eq_u32 s8, 0
	s_cselect_b32 s9, s44, 6
	s_add_i32 s11, s44, 4
	s_lshl_b32 s18, s18, 4
	s_lshl_b32 s19, s8, 2
	s_add_i32 s33, s18, s19
	s_mul_i32 s12, s33, 0x4b0
	s_lshl_b32 s32, s18, 8
	s_sub_u32 s32, s32, 0x100000
	s_mov_b32 s10, 0
	v_lshl_add_u32 v253, v1, 10, s33
	v_mov_b32_e32 v254, s47
	v_cmp_eq_u32_e32 vcc, 6, v1
	s_nop 1
	v_cndmask_b32_e32 v253, v253, v254, vcc
	v_mov_b32_e32 v247, 0
	v_cmp_gt_i32_e32 vcc, s9, v1
	s_mov_b32 s18, 0xc350
	v_cmp_gt_i32_e64 s[36:37], s18, v253
	s_and_b64 vcc, vcc, s[36:37]
	s_waitcnt lgkmcnt(0)
	s_and_saveexec_b64 s[36:37], vcc
	global_load_dword v247, v253, s[38:39]
	s_mov_b64 exec, s[36:37]
	s_mov_b32 s24, s22
	s_and_b32 s25, s23, 0xffff
	s_mov_b32 s26, 0x3938700
	s_mov_b32 s27, 0x20000
	s_and_b32 s21, s21, 0xffff
	s_mov_b32 s22, 0x3938700
	s_mov_b32 s23, 0x20000
	s_mov_b32 s28, s6
	s_and_b32 s29, s7, 0xffff
	s_mov_b32 s30, 0xc35000
	s_mov_b32 s31, 0x20000
	v_lshlrev_b32_e32 v238, 4, v1
	v_mul_u32_u24_e32 v253, 0x1746, v1
	v_lshrrev_b32_e32 v253, 16, v253
	v_min_u32_e32 v253, 3, v253
	v_mul_u32_u24_e32 v254, 11, v253
	v_sub_u32_e32 v254, v1, v254
	v_lshlrev_b32_e32 v240, 3, v253
	v_mul_u32_u24_e32 v249, 0x4b0, v253
	v_lshl_add_u32 v249, v254, 4, v249
	v_add_u32_e32 v249, 0x400, v249
	v_mov_b32_e32 v255, 0x80000000
	v_cmp_gt_u32_e64 s[34:35], 44, v1
	s_nop 1
	v_cndmask_b32_e64 v239, v255, v249, s[34:35]
	v_lshl_add_u32 v250, s8, 2, v253
	v_mul_u32_u24_e32 v250, 0x4e0, v250
	v_lshl_add_u32 v250, v254, 3, v250
	v_add_u32_e32 v242, 0x200, v250
	s_mul_i32 s18, s8, 0x1380
	v_lshl_add_u32 v241, v1, 3, s18
	v_and_b32_e32 v249, 15, v1
	v_lshrrev_b32_e32 v250, 4, v1
	v_mul_u32_u24_e32 v243, 0x4e0, v249
	v_lshl_add_u32 v243, v250, 4, v243
	v_mul_u32_u24_e32 v244, 0x440, v250
	v_lshl_add_u32 v244, v249, 1, v244
	s_lshl_b32 s18, s8, 6
	s_add_i32 s18, s18, 39936
	v_add_u32_e32 v244, s18, v244
	v_lshrrev_b32_e32 v249, 4, v0
	v_and_b32_e32 v250, 15, v0
	v_mul_u32_u24_e32 v245, 0x110, v249
	v_lshl_add_u32 v245, v250, 4, v245
	v_add_u32_e32 v245, 39936, v245
	v_lshlrev_b32_e32 v246, 8, v249
	v_lshl_add_u32 v246, v250, 4, v246
	s_lshl_b32 s18, s8, 12
	s_add_i32 s18, s18, 48640
	v_lshl_add_u32 v248, v1, 4, s18
	v_cmp_gt_u32_e32 vcc, 32, v0
	s_and_saveexec_b64 s[36:37], vcc
	v_mul_u32_u24_e32 v251, 0x4e00, v249
	v_mul_u32_u24_e32 v252, 0x4e0, v250
	v_add_u32_e32 v254, v251, v252
	v_mov_b32_e32 v250, 0
	v_mov_b32_e32 v251, 0
	v_mov_b32_e32 v252, 0
	v_mov_b32_e32 v253, 0
	ds_write_b128 v254, v[250:253] offset:1200
	s_mov_b64 exec, s[36:37]
	s_lshl_b32 s18, s8, 11
	v_lshl_add_u32 v253, v1, 4, s18
	v_add_u32_e32 v254, 0x22000, v253
	global_load_dwordx4 v[178:181], v254, s[4:5]
	global_load_dwordx4 v[182:185], v254, s[4:5] offset:1024
	v_add_u32_e32 v254, 0x2000, v254
	global_load_dwordx4 v[186:189], v254, s[4:5]
	global_load_dwordx4 v[190:193], v254, s[4:5] offset:1024
	v_mov_b32_e32 v236, v253
	s_waitcnt vmcnt(4)
	v_readlane_b32 s13, v247, s10
	s_add_u32 s14, s12, 0x4b0
	s_add_u32 s15, s12, 0x960
	s_add_u32 s16, s12, 0xe10
	s_nop 1
	s_and_b32 s18, s13, 0xff
	s_cmp_eq_u32 s18, 1
	s_cselect_b32 s42, s12, 0x80000000
	s_and_b32 s18, s13, 0xff00
	s_cmp_eq_u32 s18, 0x100
	s_cselect_b32 s14, s14, 0x80000000
	s_and_b32 s18, s13, 0xff0000
	s_cmp_eq_u32 s18, 0x10000
	s_cselect_b32 s15, s15, 0x80000000
	s_and_b32 s18, s13, 0xff000000
	s_cmp_eq_u32 s18, 0x1000000
	s_cselect_b32 s16, s16, 0x80000000
	v_lshrrev_b32_e64 v249, v240, s13
	v_and_b32_e32 v249, 0xff, v249
	v_cmp_eq_u32_e32 vcc, 1, v249
	s_nop 1
	v_cndmask_b32_e32 v254, v255, v239, vcc
	buffer_load_dwordx4 v[138:141], v238, s[20:23], s42 offen sc1 nt
	buffer_load_dwordx4 v[142:145], v238, s[24:27], s42 offen sc1 nt
	buffer_load_dwordx4 v[146:149], v238, s[20:23], s14 offen sc1 nt
	buffer_load_dwordx4 v[150:153], v238, s[24:27], s14 offen sc1 nt
	buffer_load_dwordx4 v[154:157], v238, s[20:23], s15 offen sc1 nt
	buffer_load_dwordx4 v[158:161], v238, s[24:27], s15 offen sc1 nt
	buffer_load_dwordx4 v[162:165], v238, s[20:23], s16 offen sc1 nt
	buffer_load_dwordx4 v[166:169], v238, s[24:27], s16 offen sc1 nt
	buffer_load_dwordx4 v[170:173], v254, s[20:23], s12 offen sc1 nt
	buffer_load_dwordx4 v[174:177], v254, s[24:27], s12 offen sc1 nt
	s_add_u32 s12, s12, 0x12c000
	s_add_u32 s32, s32, 0x40000
	s_mov_b32 s19, 0x80000000
	buffer_store_dwordx4 v[226:229], v246, s[28:31], s19 offen sc1
	s_mov_b32 s10, 1
	global_load_dwordx4 v[2:5], v236, s[4:5]
	global_load_dwordx4 v[6:9], v236, s[4:5] offset:1024
	v_add_u32_e32 v236, 0x2000, v236
	global_load_dwordx4 v[10:13], v236, s[4:5]
	global_load_dwordx4 v[14:17], v236, s[4:5] offset:1024
	v_add_u32_e32 v236, 0x2000, v236
	global_load_dwordx4 v[18:21], v236, s[4:5]
	global_load_dwordx4 v[22:25], v236, s[4:5] offset:1024
	v_add_u32_e32 v236, 0x2000, v236
	global_load_dwordx4 v[26:29], v236, s[4:5]
	global_load_dwordx4 v[30:33], v236, s[4:5] offset:1024
	v_add_u32_e32 v236, 0x2000, v236
	global_load_dwordx4 v[34:37], v236, s[4:5]
	global_load_dwordx4 v[38:41], v236, s[4:5] offset:1024
	v_add_u32_e32 v236, 0x2000, v236
	global_load_dwordx4 v[42:45], v236, s[4:5]
	global_load_dwordx4 v[46:49], v236, s[4:5] offset:1024
	v_add_u32_e32 v236, 0x2000, v236
	global_load_dwordx4 v[50:53], v236, s[4:5]
	global_load_dwordx4 v[54:57], v236, s[4:5] offset:1024
	v_add_u32_e32 v236, 0x2000, v236
	global_load_dwordx4 v[58:61], v236, s[4:5]
	global_load_dwordx4 v[62:65], v236, s[4:5] offset:1024
	v_add_u32_e32 v236, 0x2000, v236
	global_load_dwordx4 v[66:69], v236, s[4:5]
	global_load_dwordx4 v[70:73], v236, s[4:5] offset:1024
	v_add_u32_e32 v236, 0x2000, v236
	global_load_dwordx4 v[74:77], v236, s[4:5]
	global_load_dwordx4 v[78:81], v236, s[4:5] offset:1024
	v_add_u32_e32 v236, 0x2000, v236
	global_load_dwordx4 v[82:85], v236, s[4:5]
	global_load_dwordx4 v[86:89], v236, s[4:5] offset:1024
	v_add_u32_e32 v236, 0x2000, v236
	global_load_dwordx4 v[90:93], v236, s[4:5]
	global_load_dwordx4 v[94:97], v236, s[4:5] offset:1024
	v_add_u32_e32 v236, 0x2000, v236
	global_load_dwordx4 v[98:101], v236, s[4:5]
	global_load_dwordx4 v[102:105], v236, s[4:5] offset:1024
	v_add_u32_e32 v236, 0x2000, v236
	global_load_dwordx4 v[106:109], v236, s[4:5]
	global_load_dwordx4 v[110:113], v236, s[4:5] offset:1024
	v_add_u32_e32 v236, 0x2000, v236
	global_load_dwordx4 v[114:117], v236, s[4:5]
	global_load_dwordx4 v[118:121], v236, s[4:5] offset:1024
	v_add_u32_e32 v236, 0x2000, v236
	global_load_dwordx4 v[122:125], v236, s[4:5]
	global_load_dwordx4 v[126:129], v236, s[4:5] offset:1024
	v_add_u32_e32 v236, 0x2000, v236
	global_load_dwordx4 v[130:133], v236, s[4:5]
	global_load_dwordx4 v[134:137], v236, s[4:5] offset:1024
	s_waitcnt vmcnt(45)
	ds_write_b128 v248, v[178:181]
	ds_write_b128 v248, v[182:185] offset:1024
	ds_write_b128 v248, v[186:189] offset:2048
	ds_write_b128 v248, v[190:193] offset:3072
	s_waitcnt lgkmcnt(0)
	s_barrier
	s_branch .Lg_half1

.Lg_s3skip0:
	s_cmp_eq_u32 s10, 10
	s_cselect_b32 s32, s46, s32
	s_sub_u32 s18, s10, 4
	s_cmp_lt_u32 s18, s9
	s_cselect_b32 s19, s32, 0x80000000
	ds_read_b128 v[226:229], v245 offset:0
	s_add_u32 s32, s32, 0x40000
	v_readlane_b32 s13, v247, s18
	v_lshrrev_b32_e32 v249, 4, v1
	v_lshlrev_b32_e32 v249, 3, v249
	v_lshrrev_b32_e64 v249, v249, s13
	v_and_b32_e32 v249, 0xff, v249
	v_cmp_eq_u32_e32 vcc, 1, v249
	s_nop 1
	v_cndmask_b32_e32 v249, v255, v246, vcc
	s_waitcnt lgkmcnt(0)
	buffer_store_dwordx4 v[226:229], v249, s[28:31], s19 offen sc1
	s_barrier
	s_add_u32 s10, s10, 1
	s_cmp_ge_u32 s10, s11
	s_cbranch_scc1 .Lg_end

.Lg_s3skip1:
	s_cmp_eq_u32 s10, 10
	s_cselect_b32 s32, s46, s32
	s_sub_u32 s18, s10, 4
	s_cmp_lt_u32 s18, s9
	s_cselect_b32 s19, s32, 0x80000000
	ds_read_b128 v[226:229], v245 offset:4352
	s_add_u32 s32, s32, 0x40000
	v_readlane_b32 s13, v247, s18
	v_lshrrev_b32_e32 v249, 4, v1
	v_lshlrev_b32_e32 v249, 3, v249
	v_lshrrev_b32_e64 v249, v249, s13
	v_and_b32_e32 v249, 0xff, v249
	v_cmp_eq_u32_e32 vcc, 1, v249
	s_nop 1
	v_cndmask_b32_e32 v249, v255, v246, vcc
	s_waitcnt lgkmcnt(0)
	buffer_store_dwordx4 v[226:229], v249, s[28:31], s19 offen sc1
	s_barrier
	s_add_u32 s10, s10, 1
	s_cmp_lt_u32 s10, s11
	s_cbranch_scc1 .Lg_top
